# v88: v85 + M3 retention next-item L2 prefetch (one dword per 128-byte line of the next item's K/V/Q rows and states, requested during the current item)
# speedup vs baseline: 1.0049x; 1.0042x over previous
.LBB0_555:
	s_and_b32 s33, s3, 1
	s_lshl_b32 s4, s33, 1
	s_add_i32 s14, s4, s18
	s_mul_i32 s4, s10, 0x1100
	s_lshl_b32 s5, s11, 7
	s_add_i32 s45, s4, s5
	s_lshl_b32 s22, s14, 6
	v_or_b32_e32 v2, s45, v116
	v_mov_b64_e32 v[50:51], s[88:89]
	s_mul_i32 s5, s14, 0x44
	s_ashr_i32 s23, s22, 31
	v_mad_i64_i32 v[2:3], s[14:15], v2, s60, v[50:51]
	s_lshl_b64 s[14:15], s[22:23], 1
	v_mov_b32_e32 v101, v0
	v_lshl_add_u64 v[2:3], v[2:3], 0, s[14:15]
	v_or_b32_e32 v10, s45, v117
	v_lshl_add_u64 v[2:3], v[2:3], 0, v[100:101]
	v_mad_i64_i32 v[10:11], s[26:27], v10, s60, v[50:51]
	s_mul_i32 s4, s10, 0x110
	v_add_co_u32_e32 v6, vcc, s78, v2
	v_lshl_add_u64 v[10:11], v[10:11], 0, s[14:15]
	v_or_b32_e32 v18, s45, v118
	s_add_i32 s4, s4, s5
	v_addc_co_u32_e32 v7, vcc, 0, v3, vcc
	v_lshl_add_u64 v[10:11], v[10:11], 0, v[100:101]
	v_mad_i64_i32 v[18:19], s[26:27], v18, s60, v[50:51]
	s_add_i32 s4, s4, s11
	v_add_co_u32_e32 v14, vcc, s78, v10
	v_lshl_add_u64 v[18:19], v[18:19], 0, s[14:15]
	v_or_b32_e32 v26, s45, v119
	s_ashr_i32 s5, s4, 31
	v_addc_co_u32_e32 v15, vcc, 0, v11, vcc
	v_lshl_add_u64 v[18:19], v[18:19], 0, v[100:101]
	v_mad_i64_i32 v[26:27], s[26:27], v26, s60, v[50:51]
	s_lshl_b64 s[10:11], s[4:5], 13
	s_add_i32 s4, s4, 34
	v_add_co_u32_e32 v22, vcc, s78, v18
	v_lshl_add_u64 v[26:27], v[26:27], 0, s[14:15]
	s_ashr_i32 s5, s4, 31
	v_addc_co_u32_e32 v23, vcc, 0, v19, vcc
	v_lshl_add_u64 v[26:27], v[26:27], 0, v[100:101]
	s_lshl_b64 s[4:5], s[4:5], 13
	v_add_co_u32_e32 v30, vcc, s78, v26
	s_cmp_eq_u32 s33, 0
	s_nop 0
	v_addc_co_u32_e32 v31, vcc, 0, v27, vcc
	s_cselect_b64 vcc, -1, 0
	s_add_u32 s10, s66, s10
	s_addc_u32 s11, s67, s11
	s_add_u32 s4, s66, s4
	s_addc_u32 s5, s67, s5
	v_or_b32_e32 v104, s45, v109
	global_load_dwordx4 v[2:5], v[6:7], off offset:512
	s_nop 0
	global_load_dwordx4 v[6:9], v[6:7], off
	s_nop 0
	global_load_dwordx4 v[10:13], v[14:15], off offset:512
	s_nop 0
	global_load_dwordx4 v[14:17], v[14:15], off
	s_nop 0
	global_load_dwordx4 v[18:21], v[22:23], off offset:512
	s_nop 0
	global_load_dwordx4 v[22:25], v[22:23], off
	s_nop 0
	global_load_dwordx4 v[26:29], v[30:31], off offset:512
	s_nop 0
	global_load_dwordx4 v[30:33], v[30:31], off
	s_nop 0
	global_load_dwordx4 v[34:37], v125, s[10:11]
	global_load_dwordx4 v[38:41], v125, s[4:5]
	global_load_dwordx4 v[42:45], v126, s[10:11]
	global_load_dwordx4 v[46:49], v126, s[4:5]
	v_mad_i64_i32 v[106:107], s[4:5], v104, s60, v[50:51]
	v_lshl_add_u64 v[50:51], v[106:107], 0, s[14:15]
	v_mov_b32_e32 v103, v0
	v_lshl_add_u64 v[50:51], v[50:51], 0, v[102:103]
	global_load_dwordx4 v[78:81], v[50:51], off offset:3584
	global_load_dwordx4 v[74:77], v[50:51], off offset:3616
	global_load_dwordx4 v[70:73], v[50:51], off offset:3648
	global_load_dwordx4 v[66:69], v[50:51], off offset:3680
	v_cndmask_b32_e32 v50, v142, v1, vcc
	s_mov_b32 s10, 0
	v_mul_f32_e32 v101, 0xbfb8aa3b, v50
	v_ashrrev_i32_e32 v105, 31, v104
	s_mov_b64 s[4:5], -1
	s_waitcnt vmcnt(15)
	ds_write_b128 v127, v[2:5]
	s_waitcnt vmcnt(14)
	ds_write_b128 v128, v[6:9] offset:16384
	s_waitcnt vmcnt(13)
	ds_write_b128 v129, v[10:13]
	s_waitcnt vmcnt(12)
	ds_write_b128 v130, v[14:17] offset:16384
	s_waitcnt vmcnt(11)
	ds_write_b128 v127, v[18:21] offset:8192
	s_waitcnt vmcnt(10)
	ds_write_b128 v131, v[22:25] offset:16384
	s_waitcnt vmcnt(9)
	ds_write_b128 v132, v[26:29] offset:8192
	s_waitcnt vmcnt(8)
	ds_write_b128 v133, v[30:33] offset:16384
	s_waitcnt vmcnt(7)
	ds_write_b128 v128, v[34:37] offset:32768
	s_waitcnt vmcnt(6)
	ds_write_b128 v128, v[38:41] offset:40960
	s_waitcnt vmcnt(5)
	ds_write_b128 v130, v[42:45] offset:32768
	s_waitcnt vmcnt(4)
	ds_write_b128 v130, v[46:49] offset:40960
	v_cndmask_b32_e32 v2, v143, v141, vcc
	v_mov_b32_e32 v18, 0
	v_mul_f32_e32 v103, 0xbfb8aa3b, v2
	v_mul_f32_e32 v167, 0xbf800000, v101
	v_mul_f32_e32 v168, 0xc0000000, v101
	v_mul_f32_e32 v169, 0xc0400000, v101
	v_mul_f32_e32 v170, 0xc1000000, v101
	v_mul_f32_e32 v171, 0x3f800000, v103
	v_mul_f32_e32 v172, 0x40000000, v103
	v_mul_f32_e32 v173, 0x40400000, v103
	v_mul_f32_e32 v174, 0x41000000, v103
	v_exp_f32_e32 v167, v167
	v_exp_f32_e32 v168, v168
	v_exp_f32_e32 v169, v169
	v_exp_f32_e32 v170, v170
	v_exp_f32_e32 v171, v171
	v_exp_f32_e32 v172, v172
	v_exp_f32_e32 v173, v173
	v_exp_f32_e32 v174, v174
	v_mov_b32_e32 v19, v18
	v_mov_b32_e32 v20, v18
	v_mov_b32_e32 v21, v18
	v_mov_b32_e32 v22, v18
	v_mov_b32_e32 v23, v18
	v_mov_b32_e32 v24, v18
	v_mov_b32_e32 v25, v18
	v_mov_b32_e32 v26, v18
	v_mov_b32_e32 v27, v18
	v_mov_b32_e32 v28, v18
	v_mov_b32_e32 v29, v18
	v_mov_b32_e32 v30, v18
	v_mov_b32_e32 v31, v18
	v_mov_b32_e32 v32, v18
	v_mov_b32_e32 v33, v18
	v_mov_b32_e32 v2, v18
	v_mov_b32_e32 v3, v18
	v_mov_b32_e32 v4, v18
	v_mov_b32_e32 v5, v18
	v_mov_b32_e32 v6, v18
	v_mov_b32_e32 v7, v18
	v_mov_b32_e32 v8, v18
	v_mov_b32_e32 v9, v18
	v_mov_b32_e32 v10, v18
	v_mov_b32_e32 v11, v18
	v_mov_b32_e32 v12, v18
	v_mov_b32_e32 v13, v18
	v_mov_b32_e32 v14, v18
	v_mov_b32_e32 v15, v18
	v_mov_b32_e32 v16, v18
	v_mov_b32_e32 v17, v18
	s_waitcnt lgkmcnt(0)
	s_barrier
	v_lshl_add_u64 v[152:153], s[22:23], 1, v[106:107]
	v_lshlrev_b32_e32 v154, 1, v82
	v_mov_b32_e32 v155, v0
	v_lshl_add_u64 v[152:153], v[152:153], 0, v[154:155]
	s_mov_b64 s[98:99], 0x1400
	ds_read_b64 v[156:157], v0 offset:640
	v_lshl_add_u64 v[154:155], v[152:153], 0, s[98:99]
	v_add_co_u32_e32 v152, vcc, s78, v152
	s_lshl_b64 s[98:99], s[24:25], 2
	s_lshl_b64 s[100:101], s[22:23], 2
	v_addc_co_u32_e32 v153, vcc, 0, v153, vcc
	global_load_dwordx2 v[222:223], v[152:153], off offset:1024
	global_load_dwordx2 v[224:225], v[154:155], off offset:16
	global_load_dwordx2 v[226:227], v[154:155], off offset:32
	global_load_dwordx2 v[228:229], v[154:155], off offset:48
	global_load_dwordx2 v[230:231], v[154:155], off offset:64
	global_load_dwordx2 v[232:233], v[154:155], off offset:80
	global_load_dwordx2 v[234:235], v[154:155], off offset:96
	global_load_dwordx2 v[236:237], v[154:155], off offset:112
	s_add_u32 s98, s98, s100
	s_addc_u32 s99, s99, s101
	s_waitcnt lgkmcnt(0)
	v_readfirstlane_b32 s100, v156
	v_readfirstlane_b32 s101, v157
	v_lshlrev_b32_e32 v152, 2, v82
	s_add_u32 s98, s100, s98
	s_addc_u32 s99, s101, s99
	global_load_dwordx4 v[238:241], v152, s[98:99]
	global_load_dwordx4 v[242:245], v152, s[98:99] offset:32
	global_load_dwordx4 v[246:249], v152, s[98:99] offset:64
	global_load_dwordx4 v[250:253], v152, s[98:99] offset:96
	global_load_dwordx4 v[200:203], v152, s[98:99] offset:128
	global_load_dwordx4 v[204:207], v152, s[98:99] offset:160
	global_load_dwordx4 v[214:217], v152, s[98:99] offset:192
	global_load_dwordx4 v[192:195], v152, s[98:99] offset:224
	s_add_i32 vcc_lo, s3, s65
	s_cmp_ge_i32 vcc_lo, s81
	s_cbranch_scc1 .Lm3r_pf_none
	s_and_b64 s[100:101], exec, s[94:95]
	s_cbranch_scc0 .Lm3r_pf_ctx
	s_bfe_u32 vcc_hi, vcc_lo, 0x50001
	s_add_i32 vcc_hi, vcc_hi, 2
	s_ashr_i32 s98, vcc_lo, 6
	s_branch .Lm3r_pf_bc
.Lm3r_pf_ctx:
	s_bfe_u32 vcc_hi, vcc_lo, 0x10001
	s_ashr_i32 s98, vcc_lo, 2
.Lm3r_pf_bc:
	s_and_b32 s99, vcc_lo, 1
	s_lshl_b32 s99, s99, 1
	s_add_i32 s99, s99, s18
	s_mul_i32 s100, s98, 0x1100
	s_lshl_b32 s101, vcc_hi, 7
	s_add_i32 s100, s100, s101
	s_and_b32 s101, s47, 1
	s_lshl_b32 s101, s101, 6
	v_mbcnt_lo_u32_b32 v154, -1, 0
	v_mbcnt_hi_u32_b32 v154, -1, v154
	v_or_b32_e32 v154, s101, v154
	v_add_u32_e32 v155, s100, v154
	v_mul_u32_u24_e32 v155, 0x1600, v155
	s_lshl_b32 s101, s99, 7
	s_bitcmp1_b32 s47, 1
	s_cbranch_scc1 .Lm3r_pf_sel1
	s_addk_i32 s101, 0x1000
	v_add_u32_e32 v155, s101, v155
	global_load_dword v208, v155, s[88:89]
	global_load_dword v209, v155, s[88:89] offset:-512
	s_branch .Lm3r_pf_done
.Lm3r_pf_sel1:
	s_addk_i32 s101, 0x1200
	v_add_u32_e32 v155, s101, v155
	global_load_dword v208, v155, s[88:89]
	s_mul_i32 s100, s98, 0x110
	s_mul_i32 s101, s99, 0x44
	s_add_i32 s100, s100, s101
	s_add_i32 s100, s100, vcc_hi
	s_lshl_b32 s100, s100, 13
	v_lshrrev_b32_e32 v156, 6, v154
	v_mul_u32_u24_e32 v156, 0x44000, v156
	v_and_b32_e32 v157, 63, v154
	v_lshl_add_u32 v156, v157, 7, v156
	v_add_u32_e32 v156, s100, v156
	global_load_dword v209, v156, s[66:67]
	s_branch .Lm3r_pf_done
.Lm3r_pf_none:
	global_load_dword v208, v0, s[88:89]
	global_load_dword v209, v0, s[88:89]
.Lm3r_pf_done:
.LBB0_556:
	v_cndmask_b32_e64 v34, 0, 1, s[4:5]
	s_lshl_b32 s4, s10, 6
	v_cmp_ne_u32_e32 vcc, 1, v34
	v_or_b32_e32 v34, s4, v108
	v_lshl_add_u32 v152, v34, 7, s58
	v_add_u32_e32 v38, v152, v120
	ds_read_b128 v[34:37], v38 offset:16384
	ds_read_b128 v[50:53], v38 offset:20480
	v_add_u32_e32 v148, v152, v121
	s_waitcnt vmcnt(21) lgkmcnt(1)
	v_mfma_f32_32x32x16_bf16 v[34:49], v[34:37], v[78:81], 0
	ds_read_b128 v[144:147], v148 offset:16384
	ds_read_b128 v[148:151], v148 offset:20480
	s_waitcnt lgkmcnt(2)
	v_mfma_f32_32x32x16_bf16 v[50:65], v[50:53], v[78:81], 0
	s_waitcnt vmcnt(20) lgkmcnt(1)
	v_mfma_f32_32x32x16_bf16 v[34:49], v[144:147], v[74:77], v[34:49]
	s_waitcnt lgkmcnt(0)
	v_mfma_f32_32x32x16_bf16 v[50:65], v[148:151], v[74:77], v[50:65]
	v_add_u32_e32 v148, v152, v122
	ds_read_b128 v[144:147], v148 offset:16384
	ds_read_b128 v[148:151], v148 offset:20480
	s_waitcnt vmcnt(19) lgkmcnt(1)
	v_mfma_f32_32x32x16_bf16 v[34:49], v[144:147], v[70:73], v[34:49]
	s_waitcnt lgkmcnt(0)
	v_mfma_f32_32x32x16_bf16 v[50:65], v[148:151], v[70:73], v[50:65]
	v_add_u32_e32 v148, v152, v123
	ds_read_b128 v[144:147], v148 offset:16384
	ds_read_b128 v[148:151], v148 offset:20480
	s_waitcnt vmcnt(18) lgkmcnt(1)
	v_mfma_f32_32x32x16_bf16 v[34:49], v[144:147], v[66:69], v[34:49]
	v_or_b32_e32 v145, s4, v82
	s_waitcnt lgkmcnt(0)
	v_mfma_f32_32x32x16_bf16 v[50:65], v[148:151], v[66:69], v[50:65]
	v_sub_u32_e32 v166, v109, v145
	v_cvt_f32_i32_e32 v166, v166
	v_mul_f32_e32 v175, v101, v166
	v_mul_f32_e64 v183, -v103, v166
	v_exp_f32_e32 v175, v175
	v_exp_f32_e32 v183, v183
	s_nop 0
	v_mul_f32_e32 v176, v175, v170
	v_mul_f32_e32 v184, v183, v174
	v_mul_f32_e32 v177, v176, v170
	v_mul_f32_e32 v185, v184, v174
	v_mul_f32_e32 v178, v177, v170
	v_mul_f32_e32 v186, v185, v174
	v_mul_f32_e32 v179, v178, v170
	v_mul_f32_e32 v187, v186, v174
	v_mul_f32_e32 v180, v179, v170
	v_mul_f32_e32 v188, v187, v174
	v_mul_f32_e32 v181, v180, v170
	v_mul_f32_e32 v189, v188, v174
	v_mul_f32_e32 v182, v181, v170
	v_mul_f32_e32 v190, v189, v174
	v_min_f32_e32 v160, v175, v183
	v_mul_f32_e32 v144, v34, v160
	v_min_f32_e32 v162, v179, v187
	v_mul_f32_e32 v34, v50, v162
	v_mul_f32_e32 v164, v175, v167
	v_mul_f32_e32 v165, v183, v171
	v_min_f32_e32 v164, v164, v165
	v_mul_f32_e32 v50, v35, v164
	v_mul_f32_e32 v160, v179, v167
	v_mul_f32_e32 v161, v187, v171
	v_min_f32_e32 v160, v160, v161
	v_mul_f32_e32 v35, v51, v160
	v_mul_f32_e32 v162, v175, v168
	v_mul_f32_e32 v163, v183, v172
	v_min_f32_e32 v162, v162, v163
	v_mul_f32_e32 v51, v36, v162
	v_mul_f32_e32 v164, v179, v168
	v_mul_f32_e32 v165, v187, v172
	v_min_f32_e32 v164, v164, v165
	v_mul_f32_e32 v36, v52, v164
	v_mul_f32_e32 v160, v175, v169
	v_mul_f32_e32 v161, v183, v173
	v_min_f32_e32 v160, v160, v161
	v_mul_f32_e32 v52, v37, v160
	v_mul_f32_e32 v162, v179, v169
	v_mul_f32_e32 v163, v187, v173
	v_min_f32_e32 v162, v162, v163
	v_mul_f32_e32 v37, v53, v162
	v_min_f32_e32 v164, v176, v184
	v_mul_f32_e32 v53, v38, v164
	v_min_f32_e32 v160, v180, v188
	v_mul_f32_e32 v38, v54, v160
	v_mul_f32_e32 v162, v176, v167
	v_mul_f32_e32 v163, v184, v171
	v_min_f32_e32 v162, v162, v163
	v_mul_f32_e32 v54, v39, v162
	v_mul_f32_e32 v164, v180, v167
	v_mul_f32_e32 v165, v188, v171
	v_min_f32_e32 v164, v164, v165
	v_mul_f32_e32 v39, v55, v164
	v_mul_f32_e32 v160, v176, v168
	v_mul_f32_e32 v161, v184, v172
	v_min_f32_e32 v160, v160, v161
	v_mul_f32_e32 v55, v40, v160
	v_mul_f32_e32 v162, v180, v168
	v_mul_f32_e32 v163, v188, v172
	v_min_f32_e32 v162, v162, v163
	v_mul_f32_e32 v40, v56, v162
	v_mul_f32_e32 v164, v176, v169
	v_mul_f32_e32 v165, v184, v173
	v_min_f32_e32 v164, v164, v165
	v_mul_f32_e32 v56, v41, v164
	v_mul_f32_e32 v160, v180, v169
	v_mul_f32_e32 v161, v188, v173
	v_min_f32_e32 v160, v160, v161
	v_mul_f32_e32 v41, v57, v160
	v_min_f32_e32 v162, v177, v185
	v_mul_f32_e32 v57, v42, v162
	v_min_f32_e32 v164, v181, v189
	v_mul_f32_e32 v42, v58, v164
	v_mul_f32_e32 v160, v177, v167
	v_mul_f32_e32 v161, v185, v171
	v_min_f32_e32 v160, v160, v161
	v_mul_f32_e32 v43, v43, v160
	v_mul_f32_e32 v162, v181, v167
	v_mul_f32_e32 v163, v189, v171
	v_min_f32_e32 v162, v162, v163
	v_mul_f32_e32 v58, v59, v162
	v_mul_f32_e32 v164, v177, v168
	v_mul_f32_e32 v165, v185, v172
	v_min_f32_e32 v164, v164, v165
	v_mul_f32_e32 v59, v44, v164
	v_mul_f32_e32 v160, v181, v168
	v_mul_f32_e32 v161, v189, v172
	v_min_f32_e32 v160, v160, v161
	v_mul_f32_e32 v60, v60, v160
	v_mul_f32_e32 v162, v177, v169
	v_mul_f32_e32 v163, v185, v173
	v_min_f32_e32 v162, v162, v163
	v_mul_f32_e32 v147, v45, v162
	v_mul_f32_e32 v164, v181, v169
	v_mul_f32_e32 v165, v189, v173
	v_min_f32_e32 v164, v164, v165
	v_mul_f32_e32 v61, v61, v164
	v_min_f32_e32 v160, v178, v186
	v_mul_f32_e32 v146, v46, v160
	v_min_f32_e32 v162, v182, v190
	v_mul_f32_e32 v62, v62, v162
	v_mul_f32_e32 v164, v178, v167
	v_mul_f32_e32 v165, v186, v171
	v_min_f32_e32 v164, v164, v165
	v_mul_f32_e32 v148, v47, v164
	v_mul_f32_e32 v160, v182, v167
	v_mul_f32_e32 v161, v190, v171
	v_min_f32_e32 v160, v160, v161
	v_mul_f32_e32 v63, v63, v160
	v_mul_f32_e32 v162, v178, v168
	v_mul_f32_e32 v163, v186, v172
	v_min_f32_e32 v162, v162, v163
	v_mul_f32_e32 v149, v48, v162
	v_mul_f32_e32 v164, v182, v168
	v_mul_f32_e32 v165, v190, v172
	v_min_f32_e32 v164, v164, v165
	v_mul_f32_e32 v64, v64, v164
	v_mul_f32_e32 v160, v178, v169
	v_mul_f32_e32 v161, v186, v173
	v_min_f32_e32 v160, v160, v161
	v_mul_f32_e32 v145, v49, v160
	v_mul_f32_e32 v162, v182, v169
	v_mul_f32_e32 v163, v190, v173
	v_min_f32_e32 v162, v162, v163
	v_mul_f32_e32 v65, v65, v162
	v_cvt_pk_bf16_f32 v44, v144, v50
	v_cvt_pk_bf16_f32 v45, v51, v52
	v_cvt_pk_bf16_f32 v46, v53, v54
	v_cvt_pk_bf16_f32 v47, v55, v56
	v_cvt_pk_bf16_f32 v48, v57, v43
	v_cvt_pk_bf16_f32 v49, v59, v147
	v_cvt_pk_bf16_f32 v50, v146, v148
	v_cvt_pk_bf16_f32 v51, v149, v145
	v_cvt_pk_bf16_f32 v34, v34, v35
	v_cvt_pk_bf16_f32 v35, v36, v37
	v_cvt_pk_bf16_f32 v36, v38, v39
	v_cvt_pk_bf16_f32 v37, v40, v41
	v_cvt_pk_bf16_f32 v38, v42, v58
	v_cvt_pk_bf16_f32 v39, v60, v61
	v_cvt_pk_bf16_f32 v40, v62, v63
	v_cvt_pk_bf16_f32 v41, v64, v65
	v_lshl_add_u32 v42, s10, 13, v110
	ds_read_b64_tr_b16 v[52:53], v42 offset:0
	ds_read_b64_tr_b16 v[54:55], v42 offset:0x400
	ds_read_b64_tr_b16 v[56:57], v42 offset:0x800
	ds_read_b64_tr_b16 v[58:59], v42 offset:0xc00
	ds_read_b64_tr_b16 v[60:61], v42 offset:0x1000
	ds_read_b64_tr_b16 v[62:63], v42 offset:0x1400
	ds_read_b64_tr_b16 v[144:145], v42 offset:0x1800
	ds_read_b64_tr_b16 v[146:147], v42 offset:0x1c00
	s_waitcnt lgkmcnt(0)
	v_permlane32_swap_b32_e32 v44, v46
	v_permlane32_swap_b32_e32 v45, v47
	v_permlane32_swap_b32_e32 v48, v50
	v_permlane32_swap_b32_e32 v49, v51
	v_permlane32_swap_b32_e32 v34, v36
	v_permlane32_swap_b32_e32 v35, v37
	v_permlane32_swap_b32_e32 v38, v40
	v_permlane32_swap_b32_e32 v39, v41
	v_mfma_f32_32x32x16_bf16 v[18:33], v[52:55], v[44:47], v[18:33]
	ds_read_b64_tr_b16 v[52:53], v42 offset:0x200
	ds_read_b64_tr_b16 v[54:55], v42 offset:0x600
	v_mfma_f32_32x32x16_bf16 v[18:33], v[56:59], v[48:51], v[18:33]
	ds_read_b64_tr_b16 v[56:57], v42 offset:0xa00
	ds_read_b64_tr_b16 v[58:59], v42 offset:0xe00
	v_mfma_f32_32x32x16_bf16 v[18:33], v[60:63], v[34:37], v[18:33]
	ds_read_b64_tr_b16 v[60:61], v42 offset:0x1200
	ds_read_b64_tr_b16 v[62:63], v42 offset:0x1600
	v_mfma_f32_32x32x16_bf16 v[18:33], v[144:147], v[38:41], v[18:33]
	ds_read_b64_tr_b16 v[144:145], v42 offset:0x1a00
	ds_read_b64_tr_b16 v[146:147], v42 offset:0x1e00
	s_waitcnt lgkmcnt(0)
	v_mfma_f32_32x32x16_bf16 v[2:17], v[52:55], v[44:47], v[2:17]
	s_mov_b64 s[4:5], 0
	s_and_b64 vcc, exec, vcc
	s_mov_b32 s10, 1
	v_mfma_f32_32x32x16_bf16 v[2:17], v[56:59], v[48:51], v[2:17]
	v_mfma_f32_32x32x16_bf16 v[2:17], v[60:63], v[34:37], v[2:17]
	v_mfma_f32_32x32x16_bf16 v[2:17], v[144:147], v[38:41], v[2:17]
	s_cbranch_vccz .LBB0_556
	v_mul_f32_e32 v34, v101, v111
	v_exp_f32_e32 v50, v34
	v_mul_f32_e32 v34, v103, v112
	v_exp_f32_e32 v51, v34
	v_lshlrev_b32_e32 v35, 16, v78
	v_and_b32_e32 v36, 0xffff0000, v78
	v_mul_f32_e32 v34, v50, v35
	v_mul_f32_e32 v37, v50, v36
	v_mul_f32_e32 v36, v51, v36
	v_cvt_pk_bf16_f32 v34, v34, v37
	v_mul_f32_e32 v35, v51, v35
	v_cvt_pk_bf16_f32 v38, v35, v36
	v_lshlrev_b32_e32 v36, 16, v79
	v_and_b32_e32 v37, 0xffff0000, v79
	v_mul_f32_e32 v35, v50, v36
	v_mul_f32_e32 v39, v50, v37
	v_mul_f32_e32 v37, v51, v37
	v_cvt_pk_bf16_f32 v35, v35, v39
	v_mul_f32_e32 v36, v51, v36
	v_cvt_pk_bf16_f32 v39, v36, v37
	v_lshlrev_b32_e32 v37, 16, v80
	v_and_b32_e32 v40, 0xffff0000, v80
	v_mul_f32_e32 v36, v50, v37
	v_mul_f32_e32 v41, v50, v40
	v_cvt_pk_bf16_f32 v36, v36, v41
	v_mul_f32_e32 v37, v51, v37
	v_mul_f32_e32 v40, v51, v40
	v_lshlrev_b32_e32 v41, 16, v81
	v_and_b32_e32 v42, 0xffff0000, v81
	v_cvt_pk_bf16_f32 v40, v37, v40
	v_mul_f32_e32 v37, v50, v41
	v_mul_f32_e32 v43, v50, v42
	v_mul_f32_e32 v41, v51, v41
	v_mul_f32_e32 v42, v51, v42
	v_cvt_pk_bf16_f32 v37, v37, v43
	v_cvt_pk_bf16_f32 v41, v41, v42
	ds_read_b128 v[42:45], v134 offset:32768
	ds_read_b128 v[46:49], v134 offset:40960
	s_waitcnt lgkmcnt(1)
	v_mfma_f32_32x32x16_bf16 v[18:33], v[42:45], v[34:37], v[18:33]
	s_mov_b64 s[4:5], 0x1400
	s_waitcnt lgkmcnt(0)
	v_mfma_f32_32x32x16_bf16 v[18:33], v[46:49], v[38:41], v[18:33]
	ds_read_b128 v[42:45], v134 offset:36864
	ds_read_b128 v[46:49], v134 offset:45056
	s_waitcnt lgkmcnt(1)
	v_mfma_f32_32x32x16_bf16 v[2:17], v[42:45], v[34:37], v[2:17]
	v_lshlrev_b32_e32 v35, 16, v74
	v_and_b32_e32 v36, 0xffff0000, v74
	v_mul_f32_e32 v34, v50, v35
	v_mul_f32_e32 v37, v50, v36
	v_mul_f32_e32 v36, v51, v36
	v_cvt_pk_bf16_f32 v34, v34, v37
	v_mul_f32_e32 v35, v51, v35
	s_waitcnt lgkmcnt(0)
	v_mfma_f32_32x32x16_bf16 v[2:17], v[46:49], v[38:41], v[2:17]
	v_cvt_pk_bf16_f32 v38, v35, v36
	v_lshlrev_b32_e32 v36, 16, v75
	v_and_b32_e32 v37, 0xffff0000, v75
	v_mul_f32_e32 v35, v50, v36
	v_mul_f32_e32 v39, v50, v37
	v_mul_f32_e32 v37, v51, v37
	v_cvt_pk_bf16_f32 v35, v35, v39
	v_mul_f32_e32 v36, v51, v36
	v_cvt_pk_bf16_f32 v39, v36, v37
	v_lshlrev_b32_e32 v37, 16, v76
	v_and_b32_e32 v40, 0xffff0000, v76
	v_mul_f32_e32 v36, v50, v37
	v_mul_f32_e32 v41, v50, v40
	v_cvt_pk_bf16_f32 v36, v36, v41
	v_mul_f32_e32 v37, v51, v37
	v_mul_f32_e32 v40, v51, v40
	v_lshlrev_b32_e32 v41, 16, v77
	v_and_b32_e32 v42, 0xffff0000, v77
	v_cvt_pk_bf16_f32 v40, v37, v40
	v_mul_f32_e32 v37, v50, v41
	v_mul_f32_e32 v43, v50, v42
	v_mul_f32_e32 v41, v51, v41
	v_mul_f32_e32 v42, v51, v42
	v_cvt_pk_bf16_f32 v37, v37, v43
	v_cvt_pk_bf16_f32 v41, v41, v42
	ds_read_b128 v[42:45], v135 offset:32768
	ds_read_b128 v[46:49], v135 offset:40960
	s_waitcnt lgkmcnt(1)
	v_mfma_f32_32x32x16_bf16 v[18:33], v[42:45], v[34:37], v[18:33]
	s_waitcnt lgkmcnt(0)
	v_mfma_f32_32x32x16_bf16 v[18:33], v[46:49], v[38:41], v[18:33]
	ds_read_b128 v[42:45], v135 offset:36864
	ds_read_b128 v[46:49], v135 offset:45056
	s_waitcnt lgkmcnt(1)
	v_mfma_f32_32x32x16_bf16 v[2:17], v[42:45], v[34:37], v[2:17]
	v_lshlrev_b32_e32 v35, 16, v70
	v_and_b32_e32 v36, 0xffff0000, v70
	v_mul_f32_e32 v34, v50, v35
	v_mul_f32_e32 v37, v50, v36
	v_mul_f32_e32 v36, v51, v36
	v_cvt_pk_bf16_f32 v34, v34, v37
	v_mul_f32_e32 v35, v51, v35
	s_waitcnt lgkmcnt(0)
	v_mfma_f32_32x32x16_bf16 v[2:17], v[46:49], v[38:41], v[2:17]
	v_cvt_pk_bf16_f32 v38, v35, v36
	v_lshlrev_b32_e32 v36, 16, v71
	v_and_b32_e32 v37, 0xffff0000, v71
	v_mul_f32_e32 v35, v50, v36
	v_mul_f32_e32 v39, v50, v37
	v_mul_f32_e32 v37, v51, v37
	v_cvt_pk_bf16_f32 v35, v35, v39
	v_mul_f32_e32 v36, v51, v36
	v_cvt_pk_bf16_f32 v39, v36, v37
	v_lshlrev_b32_e32 v37, 16, v72
	v_and_b32_e32 v40, 0xffff0000, v72
	v_mul_f32_e32 v36, v50, v37
	v_mul_f32_e32 v41, v50, v40
	v_cvt_pk_bf16_f32 v36, v36, v41
	v_mul_f32_e32 v37, v51, v37
	v_mul_f32_e32 v40, v51, v40
	v_lshlrev_b32_e32 v41, 16, v73
	v_and_b32_e32 v42, 0xffff0000, v73
	v_cvt_pk_bf16_f32 v40, v37, v40
	v_mul_f32_e32 v37, v50, v41
	v_mul_f32_e32 v43, v50, v42
	v_mul_f32_e32 v41, v51, v41
	v_mul_f32_e32 v42, v51, v42
	v_cvt_pk_bf16_f32 v37, v37, v43
	v_cvt_pk_bf16_f32 v41, v41, v42
	ds_read_b128 v[42:45], v136 offset:32768
	ds_read_b128 v[46:49], v136 offset:40960
	s_waitcnt lgkmcnt(1)
	v_mfma_f32_32x32x16_bf16 v[18:33], v[42:45], v[34:37], v[18:33]
	s_waitcnt lgkmcnt(0)
	v_mfma_f32_32x32x16_bf16 v[18:33], v[46:49], v[38:41], v[18:33]
	ds_read_b128 v[42:45], v136 offset:36864
	ds_read_b128 v[46:49], v136 offset:45056
	s_waitcnt lgkmcnt(1)
	v_mfma_f32_32x32x16_bf16 v[2:17], v[42:45], v[34:37], v[2:17]
	v_lshlrev_b32_e32 v35, 16, v66
	v_and_b32_e32 v36, 0xffff0000, v66
	v_mul_f32_e32 v34, v50, v35
	v_mul_f32_e32 v37, v50, v36
	v_mul_f32_e32 v36, v51, v36
	v_cvt_pk_bf16_f32 v34, v34, v37
	v_mul_f32_e32 v35, v51, v35
	s_waitcnt lgkmcnt(0)
	v_mfma_f32_32x32x16_bf16 v[2:17], v[46:49], v[38:41], v[2:17]
	v_cvt_pk_bf16_f32 v38, v35, v36
	v_lshlrev_b32_e32 v36, 16, v67
	v_and_b32_e32 v37, 0xffff0000, v67
	v_mul_f32_e32 v35, v50, v36
	v_mul_f32_e32 v39, v50, v37
	v_mul_f32_e32 v37, v51, v37
	v_cvt_pk_bf16_f32 v35, v35, v39
	v_mul_f32_e32 v36, v51, v36
	v_cvt_pk_bf16_f32 v39, v36, v37
	v_lshlrev_b32_e32 v37, 16, v68
	v_and_b32_e32 v40, 0xffff0000, v68
	v_mul_f32_e32 v36, v50, v37
	v_mul_f32_e32 v41, v50, v40
	v_cvt_pk_bf16_f32 v36, v36, v41
	v_mul_f32_e32 v37, v51, v37
	v_mul_f32_e32 v40, v51, v40
	v_lshlrev_b32_e32 v41, 16, v69
	v_and_b32_e32 v42, 0xffff0000, v69
	v_cvt_pk_bf16_f32 v40, v37, v40
	v_mul_f32_e32 v37, v50, v41
	v_mul_f32_e32 v43, v50, v42
	v_mul_f32_e32 v41, v51, v41
	v_mul_f32_e32 v42, v51, v42
	v_cvt_pk_bf16_f32 v37, v37, v43
	v_cvt_pk_bf16_f32 v41, v41, v42
	ds_read_b128 v[42:45], v137 offset:32768
	ds_read_b128 v[46:49], v137 offset:40960
	s_waitcnt lgkmcnt(1)
	v_mfma_f32_32x32x16_bf16 v[18:33], v[42:45], v[34:37], v[18:33]
	s_waitcnt lgkmcnt(0)
	v_mfma_f32_32x32x16_bf16 v[18:33], v[46:49], v[38:41], v[18:33]
	ds_read_b128 v[42:45], v137 offset:36864
	ds_read_b128 v[46:49], v137 offset:45056
	s_waitcnt lgkmcnt(1)
	v_mfma_f32_32x32x16_bf16 v[2:17], v[42:45], v[34:37], v[2:17]
	s_waitcnt lgkmcnt(0)
	v_mfma_f32_32x32x16_bf16 v[2:17], v[46:49], v[38:41], v[2:17]
	s_nop 7
	v_mul_f32_e32 v78, v19, v19
	v_fmac_f32_e32 v78, v18, v18
	v_fmac_f32_e32 v78, v20, v20
	v_fmac_f32_e32 v78, v21, v21
	v_fmac_f32_e32 v78, v22, v22
	v_fmac_f32_e32 v78, v23, v23
	v_fmac_f32_e32 v78, v24, v24
	v_fmac_f32_e32 v78, v25, v25
	v_fmac_f32_e32 v78, v26, v26
	v_fmac_f32_e32 v78, v27, v27
	v_fmac_f32_e32 v78, v28, v28
	v_fmac_f32_e32 v78, v29, v29
	v_fmac_f32_e32 v78, v30, v30
	v_fmac_f32_e32 v78, v31, v31
	v_fmac_f32_e32 v78, v32, v32
	v_fmac_f32_e32 v78, v33, v33
	v_fmac_f32_e32 v78, v2, v2
	v_fmac_f32_e32 v78, v3, v3
	v_fmac_f32_e32 v78, v4, v4
	v_fmac_f32_e32 v78, v5, v5
	v_fmac_f32_e32 v78, v6, v6
	v_fmac_f32_e32 v78, v7, v7
	v_fmac_f32_e32 v78, v8, v8
	v_fmac_f32_e32 v78, v9, v9
	v_fmac_f32_e32 v78, v10, v10
	v_fmac_f32_e32 v78, v11, v11
	v_fmac_f32_e32 v78, v12, v12
	v_fmac_f32_e32 v78, v13, v13
	v_fmac_f32_e32 v78, v14, v14
	v_fmac_f32_e32 v78, v15, v15
	v_pk_mul_f32 v[62:63], v[16:17], v[16:17]
	s_and_b64 vcc, exec, s[20:21]
	v_add_f32_e32 v62, v78, v62
	v_add_f32_e32 v62, v62, v63
	v_mov_b32_e32 v63, v62
	s_nop 1
	v_permlane32_swap_b32_e32 v62, v63
	v_add_f32_e32 v62, v62, v63
	v_fmamk_f32 v62, v62, 0x3c800000, v210
	v_rsq_f32_e32 v78, v62
	v_lshlrev_b64 v[62:63], 10, v[104:105]
	v_lshl_add_u64 v[62:63], s[82:83], 0, v[62:63]
	v_lshl_add_u64 v[62:63], v[62:63], 0, s[22:23]
	v_mul_f32_e32 v78, 0x41800000, v78
	v_lshl_add_u64 v[62:63], v[62:63], 0, v[84:85]
	v_rcp_f32_e32 v152, v78
	s_waitcnt vmcnt(7)
	v_lshlrev_b32_e32 v153, 16, v222
	v_and_b32_e32 v154, 0xffff0000, v222
	v_lshlrev_b32_e32 v155, 16, v223
	v_and_b32_e32 v156, 0xffff0000, v223
	v_mul_f32_e32 v157, 0xbfb8aa3b, v153
	v_mul_f32_e32 v158, 0xbfb8aa3b, v154
	v_mul_f32_e32 v159, 0xbfb8aa3b, v155
	v_mul_f32_e32 v160, 0xbfb8aa3b, v156
	v_exp_f32_e32 v157, v157
	v_exp_f32_e32 v158, v158
	v_exp_f32_e32 v159, v159
	v_exp_f32_e32 v160, v160
	v_mul_f32_e32 v161, v18, v238
	v_mul_f32_e32 v162, v19, v239
	v_mul_f32_e32 v163, v20, v240
	v_mul_f32_e32 v164, v21, v241
	v_fma_f32 v157, v157, v152, v152
	v_fma_f32 v158, v158, v152, v152
	v_fma_f32 v159, v159, v152, v152
	v_fma_f32 v160, v160, v152, v152
	v_rcp_f32_e32 v157, v157
	v_rcp_f32_e32 v158, v158
	v_rcp_f32_e32 v159, v159
	v_rcp_f32_e32 v160, v160
	v_mul_f32_e32 v153, v153, v157
	v_mul_f32_e32 v154, v154, v158
	v_mul_f32_e32 v155, v155, v159
	v_mul_f32_e32 v156, v156, v160
	v_mul_f32_e32 v161, v161, v153
	v_mul_f32_e32 v162, v162, v154
	v_mul_f32_e32 v163, v163, v155
	v_mul_f32_e32 v164, v164, v156
	v_cvt_pk_fp8_f32 v18, v161, v162
	v_cvt_pk_fp8_f32 v18, v163, v164 op_sel:[0,0,1]
	s_waitcnt vmcnt(6)
	v_lshlrev_b32_e32 v165, 16, v224
	v_and_b32_e32 v166, 0xffff0000, v224
	v_lshlrev_b32_e32 v167, 16, v225
	v_and_b32_e32 v168, 0xffff0000, v225
	v_mul_f32_e32 v169, 0xbfb8aa3b, v165
	v_mul_f32_e32 v170, 0xbfb8aa3b, v166
	v_mul_f32_e32 v171, 0xbfb8aa3b, v167
	v_mul_f32_e32 v172, 0xbfb8aa3b, v168
	v_exp_f32_e32 v169, v169
	v_exp_f32_e32 v170, v170
	v_exp_f32_e32 v171, v171
	v_exp_f32_e32 v172, v172
	v_mul_f32_e32 v173, v22, v242
	v_mul_f32_e32 v174, v23, v243
	v_mul_f32_e32 v175, v24, v244
	v_mul_f32_e32 v176, v25, v245
	v_fma_f32 v169, v169, v152, v152
	v_fma_f32 v170, v170, v152, v152
	v_fma_f32 v171, v171, v152, v152
	v_fma_f32 v172, v172, v152, v152
	v_rcp_f32_e32 v169, v169
	v_rcp_f32_e32 v170, v170
	v_rcp_f32_e32 v171, v171
	v_rcp_f32_e32 v172, v172
	v_mul_f32_e32 v165, v165, v169
	v_mul_f32_e32 v166, v166, v170
	v_mul_f32_e32 v167, v167, v171
	v_mul_f32_e32 v168, v168, v172
	v_mul_f32_e32 v173, v173, v165
	v_mul_f32_e32 v174, v174, v166
	v_mul_f32_e32 v175, v175, v167
	v_mul_f32_e32 v176, v176, v168
	v_cvt_pk_fp8_f32 v20, v173, v174
	v_cvt_pk_fp8_f32 v20, v175, v176 op_sel:[0,0,1]
	s_waitcnt vmcnt(5)
	v_lshlrev_b32_e32 v153, 16, v226
	v_and_b32_e32 v154, 0xffff0000, v226
	v_lshlrev_b32_e32 v155, 16, v227
	v_and_b32_e32 v156, 0xffff0000, v227
	v_mul_f32_e32 v157, 0xbfb8aa3b, v153
	v_mul_f32_e32 v158, 0xbfb8aa3b, v154
	v_mul_f32_e32 v159, 0xbfb8aa3b, v155
	v_mul_f32_e32 v160, 0xbfb8aa3b, v156
	v_exp_f32_e32 v157, v157
	v_exp_f32_e32 v158, v158
	v_exp_f32_e32 v159, v159
	v_exp_f32_e32 v160, v160
	v_mul_f32_e32 v161, v26, v246
	v_mul_f32_e32 v162, v27, v247
	v_mul_f32_e32 v163, v28, v248
	v_mul_f32_e32 v164, v29, v249
	v_fma_f32 v157, v157, v152, v152
	v_fma_f32 v158, v158, v152, v152
	v_fma_f32 v159, v159, v152, v152
	v_fma_f32 v160, v160, v152, v152
	v_rcp_f32_e32 v157, v157
	v_rcp_f32_e32 v158, v158
	v_rcp_f32_e32 v159, v159
	v_rcp_f32_e32 v160, v160
	v_mul_f32_e32 v153, v153, v157
	v_mul_f32_e32 v154, v154, v158
	v_mul_f32_e32 v155, v155, v159
	v_mul_f32_e32 v156, v156, v160
	v_mul_f32_e32 v161, v161, v153
	v_mul_f32_e32 v162, v162, v154
	v_mul_f32_e32 v163, v163, v155
	v_mul_f32_e32 v164, v164, v156
	v_cvt_pk_fp8_f32 v19, v161, v162
	v_cvt_pk_fp8_f32 v19, v163, v164 op_sel:[0,0,1]
	s_waitcnt vmcnt(4)
	v_lshlrev_b32_e32 v165, 16, v228
	v_and_b32_e32 v166, 0xffff0000, v228
	v_lshlrev_b32_e32 v167, 16, v229
	v_and_b32_e32 v168, 0xffff0000, v229
	v_mul_f32_e32 v169, 0xbfb8aa3b, v165
	v_mul_f32_e32 v170, 0xbfb8aa3b, v166
	v_mul_f32_e32 v171, 0xbfb8aa3b, v167
	v_mul_f32_e32 v172, 0xbfb8aa3b, v168
	v_exp_f32_e32 v169, v169
	v_exp_f32_e32 v170, v170
	v_exp_f32_e32 v171, v171
	v_exp_f32_e32 v172, v172
	v_mul_f32_e32 v173, v30, v250
	v_mul_f32_e32 v174, v31, v251
	v_mul_f32_e32 v175, v32, v252
	v_mul_f32_e32 v176, v33, v253
	v_fma_f32 v169, v169, v152, v152
	v_fma_f32 v170, v170, v152, v152
	v_fma_f32 v171, v171, v152, v152
	v_fma_f32 v172, v172, v152, v152
	v_rcp_f32_e32 v169, v169
	v_rcp_f32_e32 v170, v170
	v_rcp_f32_e32 v171, v171
	v_rcp_f32_e32 v172, v172
	v_mul_f32_e32 v165, v165, v169
	v_mul_f32_e32 v166, v166, v170
	v_mul_f32_e32 v167, v167, v171
	v_mul_f32_e32 v168, v168, v172
	v_mul_f32_e32 v173, v173, v165
	v_mul_f32_e32 v174, v174, v166
	v_mul_f32_e32 v175, v175, v167
	v_mul_f32_e32 v176, v176, v168
	v_cvt_pk_fp8_f32 v21, v173, v174
	v_cvt_pk_fp8_f32 v21, v175, v176 op_sel:[0,0,1]
	v_permlane32_swap_b32_e32 v18, v19
	s_nop 0
	v_permlane32_swap_b32_e32 v20, v21
	global_store_dwordx4 v[62:63], v[18:21], off offset:768
	s_waitcnt vmcnt(4)
	v_lshlrev_b32_e32 v153, 16, v230
	v_and_b32_e32 v154, 0xffff0000, v230
	v_lshlrev_b32_e32 v155, 16, v231
	v_and_b32_e32 v156, 0xffff0000, v231
	v_mul_f32_e32 v157, 0xbfb8aa3b, v153
	v_mul_f32_e32 v158, 0xbfb8aa3b, v154
	v_mul_f32_e32 v159, 0xbfb8aa3b, v155
	v_mul_f32_e32 v160, 0xbfb8aa3b, v156
	v_exp_f32_e32 v157, v157
	v_exp_f32_e32 v158, v158
	v_exp_f32_e32 v159, v159
	v_exp_f32_e32 v160, v160
	v_mul_f32_e32 v161, v2, v200
	v_mul_f32_e32 v162, v3, v201
	v_mul_f32_e32 v163, v4, v202
	v_mul_f32_e32 v164, v5, v203
	v_fma_f32 v157, v157, v152, v152
	v_fma_f32 v158, v158, v152, v152
	v_fma_f32 v159, v159, v152, v152
	v_fma_f32 v160, v160, v152, v152
	v_rcp_f32_e32 v157, v157
	v_rcp_f32_e32 v158, v158
	v_rcp_f32_e32 v159, v159
	v_rcp_f32_e32 v160, v160
	v_mul_f32_e32 v153, v153, v157
	v_mul_f32_e32 v154, v154, v158
	v_mul_f32_e32 v155, v155, v159
	v_mul_f32_e32 v156, v156, v160
	v_mul_f32_e32 v161, v161, v153
	v_mul_f32_e32 v162, v162, v154
	v_mul_f32_e32 v163, v163, v155
	v_mul_f32_e32 v164, v164, v156
	v_cvt_pk_fp8_f32 v2, v161, v162
	v_cvt_pk_fp8_f32 v2, v163, v164 op_sel:[0,0,1]
	s_waitcnt vmcnt(3)
	v_lshlrev_b32_e32 v165, 16, v232
	v_and_b32_e32 v166, 0xffff0000, v232
	v_lshlrev_b32_e32 v167, 16, v233
	v_and_b32_e32 v168, 0xffff0000, v233
	v_mul_f32_e32 v169, 0xbfb8aa3b, v165
	v_mul_f32_e32 v170, 0xbfb8aa3b, v166
	v_mul_f32_e32 v171, 0xbfb8aa3b, v167
	v_mul_f32_e32 v172, 0xbfb8aa3b, v168
	v_exp_f32_e32 v169, v169
	v_exp_f32_e32 v170, v170
	v_exp_f32_e32 v171, v171
	v_exp_f32_e32 v172, v172
	v_mul_f32_e32 v173, v6, v204
	v_mul_f32_e32 v174, v7, v205
	v_mul_f32_e32 v175, v8, v206
	v_mul_f32_e32 v176, v9, v207
	v_fma_f32 v169, v169, v152, v152
	v_fma_f32 v170, v170, v152, v152
	v_fma_f32 v171, v171, v152, v152
	v_fma_f32 v172, v172, v152, v152
	v_rcp_f32_e32 v169, v169
	v_rcp_f32_e32 v170, v170
	v_rcp_f32_e32 v171, v171
	v_rcp_f32_e32 v172, v172
	v_mul_f32_e32 v165, v165, v169
	v_mul_f32_e32 v166, v166, v170
	v_mul_f32_e32 v167, v167, v171
	v_mul_f32_e32 v168, v168, v172
	v_mul_f32_e32 v173, v173, v165
	v_mul_f32_e32 v174, v174, v166
	v_mul_f32_e32 v175, v175, v167
	v_mul_f32_e32 v176, v176, v168
	v_cvt_pk_fp8_f32 v4, v173, v174
	v_cvt_pk_fp8_f32 v4, v175, v176 op_sel:[0,0,1]
	s_waitcnt vmcnt(2)
	v_lshlrev_b32_e32 v153, 16, v234
	v_and_b32_e32 v154, 0xffff0000, v234
	v_lshlrev_b32_e32 v155, 16, v235
	v_and_b32_e32 v156, 0xffff0000, v235
	v_mul_f32_e32 v157, 0xbfb8aa3b, v153
	v_mul_f32_e32 v158, 0xbfb8aa3b, v154
	v_mul_f32_e32 v159, 0xbfb8aa3b, v155
	v_mul_f32_e32 v160, 0xbfb8aa3b, v156
	v_exp_f32_e32 v157, v157
	v_exp_f32_e32 v158, v158
	v_exp_f32_e32 v159, v159
	v_exp_f32_e32 v160, v160
	v_mul_f32_e32 v161, v10, v214
	v_mul_f32_e32 v162, v11, v215
	v_mul_f32_e32 v163, v12, v216
	v_mul_f32_e32 v164, v13, v217
	v_fma_f32 v157, v157, v152, v152
	v_fma_f32 v158, v158, v152, v152
	v_fma_f32 v159, v159, v152, v152
	v_fma_f32 v160, v160, v152, v152
	v_rcp_f32_e32 v157, v157
	v_rcp_f32_e32 v158, v158
	v_rcp_f32_e32 v159, v159
	v_rcp_f32_e32 v160, v160
	v_mul_f32_e32 v153, v153, v157
	v_mul_f32_e32 v154, v154, v158
	v_mul_f32_e32 v155, v155, v159
	v_mul_f32_e32 v156, v156, v160
	v_mul_f32_e32 v161, v161, v153
	v_mul_f32_e32 v162, v162, v154
	v_mul_f32_e32 v163, v163, v155
	v_mul_f32_e32 v164, v164, v156
	v_cvt_pk_fp8_f32 v3, v161, v162
	v_cvt_pk_fp8_f32 v3, v163, v164 op_sel:[0,0,1]
	s_waitcnt vmcnt(1)
	v_lshlrev_b32_e32 v165, 16, v236
	v_and_b32_e32 v166, 0xffff0000, v236
	v_lshlrev_b32_e32 v167, 16, v237
	v_and_b32_e32 v168, 0xffff0000, v237
	v_mul_f32_e32 v169, 0xbfb8aa3b, v165
	v_mul_f32_e32 v170, 0xbfb8aa3b, v166
	v_mul_f32_e32 v171, 0xbfb8aa3b, v167
	v_mul_f32_e32 v172, 0xbfb8aa3b, v168
	v_exp_f32_e32 v169, v169
	v_exp_f32_e32 v170, v170
	v_exp_f32_e32 v171, v171
	v_exp_f32_e32 v172, v172
	v_mul_f32_e32 v173, v14, v192
	v_mul_f32_e32 v174, v15, v193
	v_mul_f32_e32 v175, v16, v194
	v_mul_f32_e32 v176, v17, v195
	v_fma_f32 v169, v169, v152, v152
	v_fma_f32 v170, v170, v152, v152
	v_fma_f32 v171, v171, v152, v152
	v_fma_f32 v172, v172, v152, v152
	v_rcp_f32_e32 v169, v169
	v_rcp_f32_e32 v170, v170
	v_rcp_f32_e32 v171, v171
	v_rcp_f32_e32 v172, v172
	v_mul_f32_e32 v165, v165, v169
	v_mul_f32_e32 v166, v166, v170
	v_mul_f32_e32 v167, v167, v171
	v_mul_f32_e32 v168, v168, v172
	v_mul_f32_e32 v173, v173, v165
	v_mul_f32_e32 v174, v174, v166
	v_mul_f32_e32 v175, v175, v167
	v_mul_f32_e32 v176, v176, v168
	v_cvt_pk_fp8_f32 v5, v173, v174
	v_cvt_pk_fp8_f32 v5, v175, v176 op_sel:[0,0,1]
	v_permlane32_swap_b32_e32 v2, v3
	s_nop 0
	v_permlane32_swap_b32_e32 v4, v5
	global_store_dwordx4 v[62:63], v[2:5], off offset:800
	s_cbranch_vccz .LBB0_550
	s_waitcnt vmcnt(0)
	s_barrier
	s_and_saveexec_b64 s[4:5], s[0:1]
	s_cbranch_execz .LBB0_549
	s_mov_b64 s[10:11], exec
	v_mbcnt_lo_u32_b32 v2, s10, 0
	buffer_wbl2 sc1
	s_waitcnt vmcnt(0)
	s_waitcnt vmcnt(0)
	v_mbcnt_hi_u32_b32 v2, s11, v2
	v_cmp_eq_u32_e32 vcc, 0, v2
	s_and_b64 s[14:15], exec, vcc
	s_mov_b64 exec, s[14:15]
	s_cbranch_execz .LBB0_549
	s_bcnt1_i32_b64 s10, s[10:11]
	v_mov_b32_e32 v2, s10
	global_atomic_add v0, v2, s[84:85]
	s_branch .LBB0_549
